# PROJ K-loop LDS-DMA addressing via SGPR base + 32-bit VGPR offset (removes 16 64-bit VALU adds per loop body)
# speedup vs baseline: 1.0081x; 1.0030x over previous
; #define PG8_STAGE(bufoff, gbase, voff) do { _Pragma("unroll") for (int _i = 0; _i < 2; ++_i) \
;         __builtin_amdgcn_global_load_lds((const unsigned*)((const char*)(gbase) + (voff)[_i]), (PG8_LAS unsigned*)(lds + (bufoff) + ldsw + _i * 8192), 16, 0, 0); } while (0)
; #define PG8_LDA(dst, b, h) do { _Pragma("unroll") for (int m = 0; m < 4; ++m) _Pragma("unroll") for (int k = 0; k < 2; ++k) dst[m][k] = *(const PG8_LAS s16x8*)(lds + PG8_SA(b, h) + aoff + m * 2048 + k * 1024); } while (0)
; #define PG8_LDB(dst, b, h) do { _Pragma("unroll") for (int n = 0; n < 2; ++n) _Pragma("unroll") for (int k = 0; k < 2; ++k) dst[n][k] = *(const PG8_LAS s16x8*)(lds + PG8_SB(b, h) + boff + n * 2048 + k * 1024); } while (0)
; #define PG8_WAIT_V(n) asm volatile("s_waitcnt vmcnt(" #n ")" ::: "memory")
; #define PG8_WAIT_L(n) asm volatile("s_waitcnt lgkmcnt(" #n ")" ::: "memory")
; #define PG8_BAR __builtin_amdgcn_s_barrier()
; #define PG8_SCHED __builtin_amdgcn_sched_barrier(0)
; #define PG8_STAGE(bufoff, gbase, voff) do { _Pragma("unroll") for (int _i = 0; _i < 2; ++_i) \
;         __builtin_amdgcn_global_load_lds((const unsigned*)((const char*)(gbase) + (voff)[_i]), (PG8_LAS unsigned*)(lds + (bufoff) + ldsw + _i * 8192), 16, 0, 0); } while (0)
; #define PG8_LDA(dst, b, h) do { _Pragma("unroll") for (int m = 0; m < 4; ++m) _Pragma("unroll") for (int k = 0; k < 2; ++k) dst[m][k] = *(const PG8_LAS s16x8*)(lds + PG8_SA(b, h) + aoff + m * 2048 + k * 1024); } while (0)
; #define PG8_LDB(dst, b, h) do { _Pragma("unroll") for (int n = 0; n < 2; ++n) _Pragma("unroll") for (int k = 0; k < 2; ++k) dst[n][k] = *(const PG8_LAS s16x8*)(lds + PG8_SB(b, h) + boff + n * 2048 + k * 1024); } while (0)
; template <class Epi, class Sched, bool ALIGN_EPI = true>
; __device__ __forceinline__ void gemm_phase(PG8_LAS unsigned char* lds, const Gemm g, const Sched& S, const Epi& E) {
;     ...
;             PG8_LDB(B0, 0, 0); PG8_LDB(B1, 0, 1); PG8_SCHED; PG8_LDA(At, 0, 0); PG8_STAGE(PG8_SA(1, 1), a1 + hA, voffA);
;             PG8_WAIT_V(8); PG8_WAIT_L(0); PG8_BAR; PG8_MMA(0, 0, At, B0); PG8_MMA(0, 1, At, B1); PG8_BAR; PG8_SCHED;
;             PG8_LDA(At, 0, 1); PG8_STAGE(PG8_SB(0, 0), b2, voffB); PG8_STAGE(PG8_SB(0, 1), b2 + hB, voffB); PG8_STAGE(PG8_SA(0, 0), a2, voffA);
;             PG8_WAIT_V(8); PG8_WAIT_L(0); PG8_BAR; PG8_MMA(1, 0, At, B0); PG8_MMA(1, 1, At, B1); PG8_BAR; PG8_SCHED;
.LBB0_980:
	s_add_u32 s52, s50, 0xfffc0080
	s_addc_u32 s53, s51, -1
	s_add_i32 s57, 0, 0x10000
	s_cmp_eq_u32 s56, 12
	s_cselect_b32 s55, s36, s53
	s_cselect_b32 s54, s37, s52
	s_cselect_b32 s53, s21, s45
	s_cselect_b32 s52, s41, s44
	s_add_i32 s60, 0, 0x14000
	v_add_u32_e32 v156, s57, v141
	v_add_u32_e32 v172, s60, v141
	ds_read_b128 v[144:147], v156
	ds_read_b128 v[148:151], v156 offset:1024
	ds_read_b128 v[152:155], v156 offset:2048
	ds_read_b128 v[156:159], v156 offset:3072
	ds_read_b128 v[160:163], v172
	ds_read_b128 v[164:167], v172 offset:1024
	ds_read_b128 v[168:171], v172 offset:2048
	ds_read_b128 v[172:175], v172 offset:3072
	s_add_i32 m0, s10, 0xc000
	ds_read_b128 v[176:179], v143
	ds_read_b128 v[180:183], v143 offset:1024
	ds_read_b128 v[184:187], v143 offset:2048
	ds_read_b128 v[188:191], v143 offset:3072
	ds_read_b128 v[192:195], v143 offset:4096
	ds_read_b128 v[196:199], v143 offset:5120
	ds_read_b128 v[200:203], v143 offset:6144
	ds_read_b128 v[204:207], v143 offset:7168
	global_load_lds_dwordx4 v136, s[50:51]
	s_add_i32 m0, s10, 0xe000
	s_nop 0
	global_load_lds_dwordx4 v138, s[50:51]
	s_waitcnt vmcnt(8)
	s_waitcnt lgkmcnt(0)
	s_barrier
	s_setprio 1
	s_waitcnt lgkmcnt(0)
	v_mfma_f32_16x16x32_f16 v[126:129], v[144:147], v[176:179], v[126:129]
	v_mfma_f32_16x16x32_f16 v[122:125], v[152:155], v[176:179], v[122:125]
	v_mfma_f32_16x16x32_f16 v[118:121], v[144:147], v[184:187], v[118:121]
	v_mfma_f32_16x16x32_f16 v[114:117], v[152:155], v[184:187], v[114:117]
	v_mfma_f32_16x16x32_f16 v[102:105], v[144:147], v[192:195], v[102:105]
	v_mfma_f32_16x16x32_f16 v[98:101], v[152:155], v[192:195], v[98:101]
	v_mfma_f32_16x16x32_f16 v[84:87], v[144:147], v[200:203], v[84:87]
	v_mfma_f32_16x16x32_f16 v[80:83], v[152:155], v[200:203], v[80:83]
	v_mfma_f32_16x16x32_f16 v[126:129], v[148:151], v[180:183], v[126:129]
	v_mfma_f32_16x16x32_f16 v[122:125], v[156:159], v[180:183], v[122:125]
	v_mfma_f32_16x16x32_f16 v[118:121], v[148:151], v[188:191], v[118:121]
	v_mfma_f32_16x16x32_f16 v[114:117], v[156:159], v[188:191], v[114:117]
	v_mfma_f32_16x16x32_f16 v[102:105], v[148:151], v[196:199], v[102:105]
	v_mfma_f32_16x16x32_f16 v[98:101], v[156:159], v[196:199], v[98:101]
	v_mfma_f32_16x16x32_f16 v[84:87], v[148:151], v[204:207], v[84:87]
	v_mfma_f32_16x16x32_f16 v[80:83], v[156:159], v[204:207], v[80:83]
	s_setprio 0
	s_setprio 1
	v_mfma_f32_16x16x32_f16 v[110:113], v[160:163], v[176:179], v[110:113]
	v_mfma_f32_16x16x32_f16 v[106:109], v[168:171], v[176:179], v[106:109]
	v_mfma_f32_16x16x32_f16 v[92:95], v[160:163], v[184:187], v[92:95]
	v_mfma_f32_16x16x32_f16 v[88:91], v[168:171], v[184:187], v[88:91]
	v_mfma_f32_16x16x32_f16 v[76:79], v[160:163], v[192:195], v[76:79]
	v_mfma_f32_16x16x32_f16 v[72:75], v[168:171], v[192:195], v[72:75]
	v_mfma_f32_16x16x32_f16 v[68:71], v[160:163], v[200:203], v[68:71]
	v_mfma_f32_16x16x32_f16 v[64:67], v[168:171], v[200:203], v[64:67]
	v_mfma_f32_16x16x32_f16 v[110:113], v[164:167], v[180:183], v[110:113]
	v_mfma_f32_16x16x32_f16 v[106:109], v[172:175], v[180:183], v[106:109]
	v_mfma_f32_16x16x32_f16 v[92:95], v[164:167], v[188:191], v[92:95]
	v_mfma_f32_16x16x32_f16 v[88:91], v[172:175], v[188:191], v[88:91]
	v_mfma_f32_16x16x32_f16 v[76:79], v[164:167], v[196:199], v[76:79]
	v_mfma_f32_16x16x32_f16 v[72:75], v[172:175], v[196:199], v[72:75]
	v_mfma_f32_16x16x32_f16 v[68:71], v[164:167], v[204:207], v[68:71]
	v_mfma_f32_16x16x32_f16 v[64:67], v[172:175], v[204:207], v[64:67]
	s_setprio 0
	s_barrier
	s_add_i32 s57, s57, s6
	s_mov_b32 m0, s57
	ds_read_b128 v[176:179], v143 offset:16384
	ds_read_b128 v[180:183], v143 offset:17408
	ds_read_b128 v[184:187], v143 offset:18432
	ds_read_b128 v[188:191], v143 offset:19456
	ds_read_b128 v[192:195], v143 offset:20480
	ds_read_b128 v[196:199], v143 offset:21504
	ds_read_b128 v[200:203], v143 offset:22528
	ds_read_b128 v[204:207], v143 offset:23552
	global_load_lds_dwordx4 v96, s[52:53]
	s_add_i32 m0, s57, 0x2000
	s_add_u32 s58, s52, 0x40000
	s_addc_u32 s59, s53, 0
	s_add_i32 s57, s60, s6
	global_load_lds_dwordx4 v130, s[52:53]
	s_add_u32 s100, s54, 0x80
	s_addc_u32 s101, s55, 0
	s_mov_b32 m0, s57
	s_nop 0
	global_load_lds_dwordx4 v96, s[58:59]
	s_add_i32 m0, s57, 0x2000
	s_nop 0
	global_load_lds_dwordx4 v130, s[58:59]
	s_mov_b32 m0, s10
	s_nop 0
	global_load_lds_dwordx4 v134, s[54:55]
	s_mov_b32 m0, s11
	s_nop 0
	global_load_lds_dwordx4 v132, s[54:55]
	s_waitcnt vmcnt(8)
	s_waitcnt lgkmcnt(0)
	s_barrier
	s_setprio 1
	s_waitcnt lgkmcnt(0)
	v_mfma_f32_16x16x32_f16 v[60:63], v[144:147], v[176:179], v[60:63]
	v_mfma_f32_16x16x32_f16 v[56:59], v[152:155], v[176:179], v[56:59]
	v_mfma_f32_16x16x32_f16 v[52:55], v[144:147], v[184:187], v[52:55]
	v_mfma_f32_16x16x32_f16 v[48:51], v[152:155], v[184:187], v[48:51]
	v_mfma_f32_16x16x32_f16 v[36:39], v[144:147], v[192:195], v[36:39]
	v_mfma_f32_16x16x32_f16 v[32:35], v[152:155], v[192:195], v[32:35]
	v_mfma_f32_16x16x32_f16 v[20:23], v[144:147], v[200:203], v[20:23]
	v_mfma_f32_16x16x32_f16 v[16:19], v[152:155], v[200:203], v[16:19]
	v_mfma_f32_16x16x32_f16 v[60:63], v[148:151], v[180:183], v[60:63]
	v_mfma_f32_16x16x32_f16 v[56:59], v[156:159], v[180:183], v[56:59]
	v_mfma_f32_16x16x32_f16 v[52:55], v[148:151], v[188:191], v[52:55]
	v_mfma_f32_16x16x32_f16 v[48:51], v[156:159], v[188:191], v[48:51]
	v_mfma_f32_16x16x32_f16 v[36:39], v[148:151], v[196:199], v[36:39]
	v_mfma_f32_16x16x32_f16 v[32:35], v[156:159], v[196:199], v[32:35]
	v_mfma_f32_16x16x32_f16 v[20:23], v[148:151], v[204:207], v[20:23]
	v_mfma_f32_16x16x32_f16 v[16:19], v[156:159], v[204:207], v[16:19]
	s_setprio 0
	s_setprio 1
	v_mfma_f32_16x16x32_f16 v[44:47], v[160:163], v[176:179], v[44:47]
	v_mfma_f32_16x16x32_f16 v[40:43], v[168:171], v[176:179], v[40:43]
	v_mfma_f32_16x16x32_f16 v[28:31], v[160:163], v[184:187], v[28:31]
	v_mfma_f32_16x16x32_f16 v[24:27], v[168:171], v[184:187], v[24:27]
	v_mfma_f32_16x16x32_f16 v[12:15], v[160:163], v[192:195], v[12:15]
	v_mfma_f32_16x16x32_f16 v[8:11], v[168:171], v[192:195], v[8:11]
	v_mfma_f32_16x16x32_f16 v[4:7], v[160:163], v[200:203], v[4:7]
	v_mfma_f32_16x16x32_f16 v[0:3], v[168:171], v[200:203], v[0:3]
	v_mfma_f32_16x16x32_f16 v[44:47], v[164:167], v[180:183], v[44:47]
	v_mfma_f32_16x16x32_f16 v[40:43], v[172:175], v[180:183], v[40:43]
	v_mfma_f32_16x16x32_f16 v[28:31], v[164:167], v[188:191], v[28:31]
	v_mfma_f32_16x16x32_f16 v[24:27], v[172:175], v[188:191], v[24:27]
	v_mfma_f32_16x16x32_f16 v[12:15], v[164:167], v[196:199], v[12:15]
	v_mfma_f32_16x16x32_f16 v[8:11], v[172:175], v[196:199], v[8:11]
	v_mfma_f32_16x16x32_f16 v[4:7], v[164:167], v[204:207], v[4:7]
	v_mfma_f32_16x16x32_f16 v[0:3], v[172:175], v[204:207], v[0:3]
	s_setprio 0
	s_barrier
; #define PG8_STAGE(bufoff, gbase, voff) do { _Pragma("unroll") for (int _i = 0; _i < 2; ++_i) \
;         __builtin_amdgcn_global_load_lds((const unsigned*)((const char*)(gbase) + (voff)[_i]), (PG8_LAS unsigned*)(lds + (bufoff) + ldsw + _i * 8192), 16, 0, 0); } while (0)
; #define PG8_LDA(dst, b, h) do { _Pragma("unroll") for (int m = 0; m < 4; ++m) _Pragma("unroll") for (int k = 0; k < 2; ++k) dst[m][k] = *(const PG8_LAS s16x8*)(lds + PG8_SA(b, h) + aoff + m * 2048 + k * 1024); } while (0)
; #define PG8_LDB(dst, b, h) do { _Pragma("unroll") for (int n = 0; n < 2; ++n) _Pragma("unroll") for (int k = 0; k < 2; ++k) dst[n][k] = *(const PG8_LAS s16x8*)(lds + PG8_SB(b, h) + boff + n * 2048 + k * 1024); } while (0)
; #define PG8_WAIT_V(n) asm volatile("s_waitcnt vmcnt(" #n ")" ::: "memory")
; #define PG8_WAIT_L(n) asm volatile("s_waitcnt lgkmcnt(" #n ")" ::: "memory")
; #define PG8_BAR __builtin_amdgcn_s_barrier()
; #define PG8_SCHED __builtin_amdgcn_sched_barrier(0)
; #define PG8_STAGE(bufoff, gbase, voff) do { _Pragma("unroll") for (int _i = 0; _i < 2; ++_i) \
;         __builtin_amdgcn_global_load_lds((const unsigned*)((const char*)(gbase) + (voff)[_i]), (PG8_LAS unsigned*)(lds + (bufoff) + ldsw + _i * 8192), 16, 0, 0); } while (0)
; #define PG8_LDA(dst, b, h) do { _Pragma("unroll") for (int m = 0; m < 4; ++m) _Pragma("unroll") for (int k = 0; k < 2; ++k) dst[m][k] = *(const PG8_LAS s16x8*)(lds + PG8_SA(b, h) + aoff + m * 2048 + k * 1024); } while (0)
; #define PG8_WAIT_V(n) asm volatile("s_waitcnt vmcnt(" #n ")" ::: "memory")
; #define PG8_WAIT_L(n) asm volatile("s_waitcnt lgkmcnt(" #n ")" ::: "memory")
; template <class Epi, class Sched, bool ALIGN_EPI = true>
; __device__ __forceinline__ void gemm_phase(PG8_LAS unsigned char* lds, const Gemm g, const Sched& S, const Epi& E) {
;     ...
;         for (int t = 0; t < nt; t += 2) {
;     ...
;             PG8_LDB(B0, 1, 0); PG8_LDB(B1, 1, 1); PG8_SCHED; PG8_LDA(At, 1, 0); PG8_STAGE(PG8_SA(0, 1), a2 + hA, voffA);
;             PG8_WAIT_V(8); PG8_WAIT_L(0); PG8_BAR; PG8_MMA(0, 0, At, B0); PG8_MMA(0, 1, At, B1); PG8_BAR; PG8_SCHED;
;             PG8_LDA(At, 1, 1); PG8_STAGE(PG8_SB(1, 0), b3, voffB); PG8_STAGE(PG8_SB(1, 1), b3 + hB, voffB); PG8_STAGE(PG8_SA(1, 0), a3, voffA);
;             PG8_WAIT_V(8); PG8_WAIT_L(0); PG8_BAR; PG8_MMA(1, 0, At, B0); PG8_MMA(1, 1, At, B1); PG8_BAR; PG8_SCHED;
	s_add_i32 s57, 0, 0x18000
	s_add_i32 s58, 0, 0x1c000
	v_add_u32_e32 v156, s57, v141
	v_add_u32_e32 v172, s58, v141
	ds_read_b128 v[144:147], v156
	ds_read_b128 v[148:151], v156 offset:1024
	ds_read_b128 v[152:155], v156 offset:2048
	ds_read_b128 v[156:159], v156 offset:3072
	ds_read_b128 v[160:163], v172
	ds_read_b128 v[164:167], v172 offset:1024
	ds_read_b128 v[168:171], v172 offset:2048
	ds_read_b128 v[172:175], v172 offset:3072
	s_add_u32 s54, s54, 0x40000
	s_addc_u32 s55, s55, 0
	s_mov_b32 m0, s12
	ds_read_b128 v[176:179], v143 offset:32768
	ds_read_b128 v[180:183], v143 offset:33792
	ds_read_b128 v[184:187], v143 offset:34816
	ds_read_b128 v[188:191], v143 offset:35840
	ds_read_b128 v[192:195], v143 offset:36864
	ds_read_b128 v[196:199], v143 offset:37888
	ds_read_b128 v[200:203], v143 offset:38912
	ds_read_b128 v[204:207], v143 offset:39936
	global_load_lds_dwordx4 v134, s[54:55]
	s_mov_b32 m0, s13
	s_nop 0
	global_load_lds_dwordx4 v132, s[54:55]
	s_waitcnt vmcnt(8)
	s_waitcnt lgkmcnt(0)
	s_barrier
	s_setprio 1
	s_waitcnt lgkmcnt(0)
	v_mfma_f32_16x16x32_f16 v[126:129], v[144:147], v[176:179], v[126:129]
	v_mfma_f32_16x16x32_f16 v[122:125], v[152:155], v[176:179], v[122:125]
	v_mfma_f32_16x16x32_f16 v[118:121], v[144:147], v[184:187], v[118:121]
	v_mfma_f32_16x16x32_f16 v[114:117], v[152:155], v[184:187], v[114:117]
	v_mfma_f32_16x16x32_f16 v[102:105], v[144:147], v[192:195], v[102:105]
	v_mfma_f32_16x16x32_f16 v[98:101], v[152:155], v[192:195], v[98:101]
	v_mfma_f32_16x16x32_f16 v[84:87], v[144:147], v[200:203], v[84:87]
	v_mfma_f32_16x16x32_f16 v[80:83], v[152:155], v[200:203], v[80:83]
	v_mfma_f32_16x16x32_f16 v[126:129], v[148:151], v[180:183], v[126:129]
	v_mfma_f32_16x16x32_f16 v[122:125], v[156:159], v[180:183], v[122:125]
	v_mfma_f32_16x16x32_f16 v[118:121], v[148:151], v[188:191], v[118:121]
	v_mfma_f32_16x16x32_f16 v[114:117], v[156:159], v[188:191], v[114:117]
	v_mfma_f32_16x16x32_f16 v[102:105], v[148:151], v[196:199], v[102:105]
	v_mfma_f32_16x16x32_f16 v[98:101], v[156:159], v[196:199], v[98:101]
	v_mfma_f32_16x16x32_f16 v[84:87], v[148:151], v[204:207], v[84:87]
	v_mfma_f32_16x16x32_f16 v[80:83], v[156:159], v[204:207], v[80:83]
	s_setprio 0
	s_setprio 1
	v_mfma_f32_16x16x32_f16 v[110:113], v[160:163], v[176:179], v[110:113]
	v_mfma_f32_16x16x32_f16 v[106:109], v[168:171], v[176:179], v[106:109]
	v_mfma_f32_16x16x32_f16 v[92:95], v[160:163], v[184:187], v[92:95]
	v_mfma_f32_16x16x32_f16 v[88:91], v[168:171], v[184:187], v[88:91]
	v_mfma_f32_16x16x32_f16 v[76:79], v[160:163], v[192:195], v[76:79]
	v_mfma_f32_16x16x32_f16 v[72:75], v[168:171], v[192:195], v[72:75]
	v_mfma_f32_16x16x32_f16 v[68:71], v[160:163], v[200:203], v[68:71]
	v_mfma_f32_16x16x32_f16 v[64:67], v[168:171], v[200:203], v[64:67]
	v_mfma_f32_16x16x32_f16 v[110:113], v[164:167], v[180:183], v[110:113]
	v_mfma_f32_16x16x32_f16 v[106:109], v[172:175], v[180:183], v[106:109]
	v_mfma_f32_16x16x32_f16 v[92:95], v[164:167], v[188:191], v[92:95]
	v_mfma_f32_16x16x32_f16 v[88:91], v[172:175], v[188:191], v[88:91]
	v_mfma_f32_16x16x32_f16 v[76:79], v[164:167], v[196:199], v[76:79]
	v_mfma_f32_16x16x32_f16 v[72:75], v[172:175], v[196:199], v[72:75]
	v_mfma_f32_16x16x32_f16 v[68:71], v[164:167], v[204:207], v[68:71]
	v_mfma_f32_16x16x32_f16 v[64:67], v[172:175], v[204:207], v[64:67]
	s_setprio 0
	s_barrier
	s_add_i32 s54, s57, s6
	s_add_u32 s52, s52, 0x80
	s_addc_u32 s53, s53, 0
	s_mov_b32 m0, s54
	ds_read_b128 v[176:179], v143 offset:49152
	ds_read_b128 v[180:183], v143 offset:50176
	ds_read_b128 v[184:187], v143 offset:51200
	ds_read_b128 v[188:191], v143 offset:52224
	ds_read_b128 v[192:195], v143 offset:53248
	ds_read_b128 v[196:199], v143 offset:54272
	ds_read_b128 v[200:203], v143 offset:55296
	ds_read_b128 v[204:207], v143 offset:56320
	global_load_lds_dwordx4 v96, s[52:53]
	s_add_i32 m0, s54, 0x2000
	s_add_i32 s54, s58, s6
	global_load_lds_dwordx4 v130, s[52:53]
	s_add_u32 s52, s52, 0x40000
	s_addc_u32 s53, s53, 0
	s_mov_b32 m0, s54
	s_nop 0
	global_load_lds_dwordx4 v96, s[52:53]
	s_add_i32 m0, s54, 0x2000
	s_nop 0
	global_load_lds_dwordx4 v130, s[52:53]
	s_mov_b32 m0, s19
	s_nop 0
	global_load_lds_dwordx4 v134, s[100:101]
	s_mov_b32 m0, s26
	s_nop 0
	global_load_lds_dwordx4 v132, s[100:101]
	s_waitcnt vmcnt(8)
	s_waitcnt lgkmcnt(0)
	s_barrier
	s_setprio 1
	s_waitcnt lgkmcnt(0)
	v_mfma_f32_16x16x32_f16 v[60:63], v[144:147], v[176:179], v[60:63]
	v_mfma_f32_16x16x32_f16 v[56:59], v[152:155], v[176:179], v[56:59]
	v_mfma_f32_16x16x32_f16 v[52:55], v[144:147], v[184:187], v[52:55]
	v_mfma_f32_16x16x32_f16 v[48:51], v[152:155], v[184:187], v[48:51]
	v_mfma_f32_16x16x32_f16 v[36:39], v[144:147], v[192:195], v[36:39]
	v_mfma_f32_16x16x32_f16 v[32:35], v[152:155], v[192:195], v[32:35]
	v_mfma_f32_16x16x32_f16 v[20:23], v[144:147], v[200:203], v[20:23]
	v_mfma_f32_16x16x32_f16 v[16:19], v[152:155], v[200:203], v[16:19]
	v_mfma_f32_16x16x32_f16 v[60:63], v[148:151], v[180:183], v[60:63]
	v_mfma_f32_16x16x32_f16 v[56:59], v[156:159], v[180:183], v[56:59]
	v_mfma_f32_16x16x32_f16 v[52:55], v[148:151], v[188:191], v[52:55]
	v_mfma_f32_16x16x32_f16 v[48:51], v[156:159], v[188:191], v[48:51]
	v_mfma_f32_16x16x32_f16 v[36:39], v[148:151], v[196:199], v[36:39]
	v_mfma_f32_16x16x32_f16 v[32:35], v[156:159], v[196:199], v[32:35]
	v_mfma_f32_16x16x32_f16 v[20:23], v[148:151], v[204:207], v[20:23]
	v_mfma_f32_16x16x32_f16 v[16:19], v[156:159], v[204:207], v[16:19]
	s_setprio 0
	s_setprio 1
	v_mfma_f32_16x16x32_f16 v[44:47], v[160:163], v[176:179], v[44:47]
	v_mfma_f32_16x16x32_f16 v[40:43], v[168:171], v[176:179], v[40:43]
	v_mfma_f32_16x16x32_f16 v[28:31], v[160:163], v[184:187], v[28:31]
	v_mfma_f32_16x16x32_f16 v[24:27], v[168:171], v[184:187], v[24:27]
	v_mfma_f32_16x16x32_f16 v[12:15], v[160:163], v[192:195], v[12:15]
	v_mfma_f32_16x16x32_f16 v[8:11], v[168:171], v[192:195], v[8:11]
	v_mfma_f32_16x16x32_f16 v[4:7], v[160:163], v[200:203], v[4:7]
	v_mfma_f32_16x16x32_f16 v[0:3], v[168:171], v[200:203], v[0:3]
	v_mfma_f32_16x16x32_f16 v[44:47], v[164:167], v[180:183], v[44:47]
	v_mfma_f32_16x16x32_f16 v[40:43], v[172:175], v[180:183], v[40:43]
	v_mfma_f32_16x16x32_f16 v[28:31], v[164:167], v[188:191], v[28:31]
	v_mfma_f32_16x16x32_f16 v[24:27], v[172:175], v[188:191], v[24:27]
	v_mfma_f32_16x16x32_f16 v[12:15], v[164:167], v[196:199], v[12:15]
	v_mfma_f32_16x16x32_f16 v[8:11], v[172:175], v[196:199], v[8:11]
	v_mfma_f32_16x16x32_f16 v[4:7], v[164:167], v[204:207], v[4:7]
	v_mfma_f32_16x16x32_f16 v[0:3], v[172:175], v[204:207], v[0:3]
	s_setprio 0
	s_barrier
	s_add_i32 s56, s56, 2
	s_add_u32 s50, s50, 0x100
	s_addc_u32 s51, s51, 0
	s_add_u32 s44, s44, 0x100
	s_addc_u32 s45, s45, 0
	s_cmp_gt_u32 s56, 13
	s_cbranch_scc0 .LBB0_980
	s_and_b64 vcc, exec, s[14:15]
	s_cbranch_vccz .LBB0_983
	s_barrier
